# GEMM2 operand tiles staged with full-line LDS-DMA pieces (8 rows x 128 B, xor-swizzled image, two read bases) on top of v017
# speedup vs baseline: 1.0063x; 1.0063x over previous
.LBB0_1340:
	s_andn2_b64 vcc, exec, s[0:1]
	s_cbranch_vccnz .LBB0_1423
	v_readlane_b32 s0, v253, 0
	v_readlane_b32 s1, v253, 1
	v_mov_b32_e32 v4, v0
	s_movk_i32 s6, 0x3c0
	v_readfirstlane_b32 s8, v4
	v_and_b32_e32 v2, 48, v4
	v_lshlrev_b32_e32 v3, 6, v4
	s_ashr_i32 s4, s8, 6
	s_ashr_i32 s10, s8, 8
	v_and_or_b32 v3, v3, s6, v2
	v_lshlrev_b32_e32 v2, 2, v4
	s_and_b32 s9, s4, 3
	s_lshl_b32 s5, s10, 13
	v_and_b32_e32 v5, 32, v2
	v_bitop3_b32 v2, v3, s5, v5 bitop3:0xde
	s_lshl_b32 s5, s9, 12
	v_readlane_b32 s6, v254, 44
	v_bitop3_b32 v3, v3, s5, v5 bitop3:0xde
	v_readlane_b32 s7, v254, 45
	v_or_b32_e32 v3, 0x10000, v3
	s_andn2_b64 vcc, exec, s[6:7]
	s_cbranch_vccnz .LBB0_1357
	s_load_dwordx2 s[6:7], s[0:1], 0xa0
	v_lshlrev_b32_e32 v5, 4, v4
	v_and_b32_e32 v6, 32, v4
	v_lshrrev_b32_e32 v7, 3, v4
	v_bfe_u32 v9, v5, 6, 4
	s_waitcnt lgkmcnt(0)
	s_add_u32 s14, s6, 0x47e00000
	s_addc_u32 s15, s7, 0
	s_lshl_b32 s0, s52, 26
	s_add_u32 s0, s6, s0
	s_addc_u32 s1, s7, 0
	s_add_u32 s16, s0, 0x23900000
	s_mov_b32 s0, 0x1ffff0
	v_bfe_u32 v8, v4, 2, 26
	v_and_or_b32 v7, v7, s0, v9
	v_bitop3_b32 v6, v5, v6, 48 bitop3:0x6c
	v_lshrrev_b32_e32 v9, 1, v4
	v_lshrrev_b32_e32 v10, 5, v4
	v_bfe_u32 v5, v5, 6, 2
	s_addc_u32 s17, s1, 0
	v_and_b32_e32 v8, 0x1fffc0, v8
	v_and_b32_e32 v9, 24, v9
	v_and_or_b32 v5, v10, 4, v5
	s_lshl_b32 s0, s4, 10
	v_readlane_b32 s4, v254, 53
	v_or3_b32 v5, v5, v9, v8
	v_and_or_b32 v4, v4, 64, v6
	v_readlane_b32 s5, v254, 54
	s_add_u32 s4, s16, s4
	v_lshl_or_b32 v139, v5, 11, v4
	s_addc_u32 s5, s17, s5
	s_add_i32 s24, s0, 0
	v_lshl_or_b32 v138, v7, 11, v4
	v_lshrrev_b32_e32 v201, 3, v0
	v_and_b32_e32 v202, 6, v201
	v_and_b32_e32 v203, 7, v0
	v_xor_b32_e32 v202, v202, v203
	v_lshlrev_b32_e32 v202, 4, v202
	v_lshl_or_b32 v138, v201, 11, v202
	v_bfe_u32 v201, v0, 3, 2
	v_bfe_u32 v203, v0, 7, 1
	v_lshl_or_b32 v201, v203, 2, v201
	v_bfe_u32 v203, v0, 5, 2
	v_lshl_or_b32 v201, v203, 3, v201
	v_bfe_u32 v203, v0, 8, 1
	v_lshl_or_b32 v201, v203, 6, v201
	v_lshl_or_b32 v139, v201, 11, v202
	s_add_i32 s25, s24, 0x10000
	s_mov_b64 s[0:1], s[4:5]
	v_mov_b32_e32 v4, v139
	s_mov_b32 m0, s25
	s_nop 0
	global_load_lds_dwordx4 v4, s[0:1]
	s_add_u32 s0, s4, 0x40000
	s_addc_u32 s1, s5, 0
	v_mov_b32_e32 v4, v139
	s_add_i32 s26, s24, 0x12000
	s_mov_b32 m0, s26
	s_add_i32 s27, s24, 0x14000
	global_load_lds_dwordx4 v4, s[0:1]
	s_add_u32 s0, s4, 0x10000
	s_addc_u32 s1, s5, 0
	v_mov_b32_e32 v4, v139
	s_mov_b32 m0, s27
	s_nop 0
	global_load_lds_dwordx4 v4, s[0:1]
	s_add_u32 s0, s4, 0x50000
	s_addc_u32 s1, s5, 0
	v_mov_b32_e32 v4, v139
	s_add_i32 s28, s24, 0x16000
	s_mov_b32 m0, s28
	s_nop 0
	global_load_lds_dwordx4 v4, s[0:1]
	v_readlane_b32 s0, v254, 49
	v_readlane_b32 s1, v254, 50
	s_add_u32 s0, s14, s0
	s_addc_u32 s1, s15, s1
	s_mov_b64 s[12:13], s[0:1]
	v_mov_b32_e32 v4, v138
	s_mov_b32 m0, s24
	s_nop 0
	global_load_lds_dwordx4 v4, s[12:13]
	s_add_u32 s12, s0, 0x20000
	s_addc_u32 s13, s1, 0
	v_mov_b32_e32 v4, v138
	s_add_i32 s29, s24, 0x2000
	s_mov_b32 m0, s29
	s_nop 0
	global_load_lds_dwordx4 v4, s[12:13]
	s_add_u32 s12, s0, 0x40000
	s_addc_u32 s13, s1, 0
	s_add_i32 s30, s24, 0x4000
	v_mov_b32_e32 v4, v138
	s_mov_b32 m0, s30
	s_nop 0
	global_load_lds_dwordx4 v4, s[12:13]
	s_add_u32 s12, s0, 0x60000
	s_addc_u32 s13, s1, 0
	s_add_i32 s31, s24, 0x6000
	v_mov_b32_e32 v4, v138
	s_mov_b32 m0, s31
	s_cmp_eq_u32 s10, 1
	global_load_lds_dwordx4 v4, s[12:13]
	s_cselect_b64 s[38:39], -1, 0
	s_cmp_lg_u32 s10, 1
	s_cbranch_scc1 .LBB0_1344
	s_barrier
.LBB0_1344:
	s_lshl_b32 s34, s10, 6
	s_add_u32 s40, s6, 0x57e00000
	s_addc_u32 s41, s7, 0
	s_add_u32 s42, s6, 0x37d80000
	s_addc_u32 s43, s7, 0
	s_add_u32 s6, s4, 0x80
	s_addc_u32 s7, s5, 0
	s_add_i32 s35, s24, 0x18000
	v_mov_b32_e32 v4, v139
	s_waitcnt vmcnt(2)
	s_barrier
	s_mov_b32 m0, s35
	s_mov_b32 s60, 0
	global_load_lds_dwordx4 v4, s[6:7]
	s_add_u32 s6, s4, 0x40080
	s_addc_u32 s7, s5, 0
	v_mov_b32_e32 v4, v139
	s_add_i32 s36, s24, 0x1a000
	s_mov_b32 m0, s36
	v_and_b32_e32 v201, 7, v0
	v_bfe_u32 v202, v0, 3, 1
	v_lshlrev_b32_e32 v201, 7, v201
	v_lshl_or_b32 v201, v202, 10, v201
	v_bfe_u32 v202, v0, 4, 2
	v_and_b32_e32 v203, 6, v0
	v_xor_b32_e32 v202, v202, v203
	v_lshl_or_b32 v201, v202, 4, v201
	v_bfe_u32 v202, v0, 6, 2
	v_lshl_or_b32 v140, v202, 12, v201
	v_or_b32_e32 v140, 0x10000, v140
	v_xor_b32_e32 v200, 64, v140
	global_load_lds_dwordx4 v4, s[6:7]
	s_add_u32 s6, s0, 0x80
	s_addc_u32 s7, s1, 0
	v_mov_b32_e32 v4, v138
	s_add_i32 s37, s24, 0x8000
	s_mov_b32 m0, s37
	v_bfe_u32 v202, v0, 8, 1
	v_lshl_or_b32 v141, v202, 13, v201
	v_xor_b32_e32 v199, 64, v141
	global_load_lds_dwordx4 v4, s[6:7]
	s_add_u32 s6, s0, 0x20080
	s_addc_u32 s7, s1, 0
	v_mov_b32_e32 v4, v138
	s_add_i32 s56, s24, 0xa000
	s_mov_b32 m0, s56
	s_add_i32 s57, s24, 0x1c000
	global_load_lds_dwordx4 v4, s[6:7]
	s_add_u32 s6, s4, 0x10080
	s_addc_u32 s7, s5, 0
	v_mov_b32_e32 v4, v139
	s_mov_b32 m0, s57
	s_nop 0
	global_load_lds_dwordx4 v4, s[6:7]
	s_add_u32 s6, s4, 0x50080
	s_addc_u32 s7, s5, 0
	s_add_i32 s58, s24, 0x1e000
	v_mov_b32_e32 v4, v139
	s_mov_b32 m0, s58
	s_cmpk_lt_u32 s8, 0x100
	global_load_lds_dwordx4 v4, s[6:7]
	v_readlane_b32 s6, v254, 51
	s_waitcnt vmcnt(6)
	v_readlane_b32 s7, v254, 52
	s_mov_b32 s10, s6
	v_readlane_b32 s6, v254, 47
	s_cselect_b64 s[44:45], -1, 0
	s_lshl_b32 s59, s9, 6
	s_mov_b32 s23, s6
	s_barrier
	v_readlane_b32 s7, v254, 48
	s_branch .LBB0_1347

.LBB0_1350:
	ds_read_b128 v[2:5], v140
	ds_read_b128 v[6:9], v200
	ds_read_b128 v[142:145], v140 offset:2048
	ds_read_b128 v[146:149], v200 offset:2048
	ds_read_b128 v[150:153], v140 offset:16384
	ds_read_b128 v[154:157], v200 offset:16384
	ds_read_b128 v[158:161], v140 offset:18432
	ds_read_b128 v[162:165], v200 offset:18432
	s_add_u32 s4, s0, 0x100
	s_addc_u32 s5, s1, 0
	s_cmp_eq_u32 s65, 12
	s_cselect_b32 s6, s61, s4
	s_cselect_b32 s7, s47, s5
	s_cselect_b32 s12, s62, s63
	s_cselect_b32 s13, s49, s64
	s_add_u32 s8, s6, 0x80
	s_addc_u32 s9, s7, 0
	s_add_u32 s66, s0, 0x40080
	s_addc_u32 s67, s1, 0
	v_mov_b32_e32 v198, v138
	s_add_i32 m0, s24, 0xc000
	ds_read_b128 v[166:169], v141
	ds_read_b128 v[170:173], v199
	ds_read_b128 v[174:177], v141 offset:2048
	ds_read_b128 v[178:181], v199 offset:2048
	ds_read_b128 v[182:185], v141 offset:4096
	ds_read_b128 v[186:189], v199 offset:4096
	ds_read_b128 v[190:193], v141 offset:6144
	ds_read_b128 v[194:197], v199 offset:6144
	s_add_u32 s0, s0, 0x60080
	global_load_lds_dwordx4 v198, s[66:67]
	s_addc_u32 s1, s1, 0
	v_mov_b32_e32 v198, v138
	s_add_i32 m0, s24, 0xe000
	s_nop 0
	global_load_lds_dwordx4 v198, s[0:1]
	s_waitcnt vmcnt(8)
	s_waitcnt lgkmcnt(0)
	s_barrier
	s_setprio 1
	s_waitcnt lgkmcnt(0)
	v_mfma_f32_16x16x128_f8f6f4 v[134:137], v[2:9], v[166:173], v[134:137]
	v_mfma_f32_16x16x128_f8f6f4 v[130:133], v[142:149], v[166:173], v[130:133]
	v_mfma_f32_16x16x128_f8f6f4 v[118:121], v[2:9], v[174:181], v[118:121]
	v_mfma_f32_16x16x128_f8f6f4 v[114:117], v[142:149], v[174:181], v[114:117]
	v_mfma_f32_16x16x128_f8f6f4 v[102:105], v[2:9], v[182:189], v[102:105]
	v_mfma_f32_16x16x128_f8f6f4 v[98:101], v[142:149], v[182:189], v[98:101]
	v_mfma_f32_16x16x128_f8f6f4 v[86:89], v[2:9], v[190:197], v[86:89]
	v_mfma_f32_16x16x128_f8f6f4 v[82:85], v[142:149], v[190:197], v[82:85]
	s_setprio 0
	s_setprio 1
	v_mfma_f32_16x16x128_f8f6f4 v[126:129], v[150:157], v[166:173], v[126:129]
	v_mfma_f32_16x16x128_f8f6f4 v[122:125], v[158:165], v[166:173], v[122:125]
	v_mfma_f32_16x16x128_f8f6f4 v[110:113], v[150:157], v[174:181], v[110:113]
	v_mfma_f32_16x16x128_f8f6f4 v[106:109], v[158:165], v[174:181], v[106:109]
	v_mfma_f32_16x16x128_f8f6f4 v[94:97], v[150:157], v[182:189], v[94:97]
	v_mfma_f32_16x16x128_f8f6f4 v[90:93], v[158:165], v[182:189], v[90:93]
	v_mfma_f32_16x16x128_f8f6f4 v[78:81], v[150:157], v[190:197], v[78:81]
	v_mfma_f32_16x16x128_f8f6f4 v[74:77], v[158:165], v[190:197], v[74:77]
	s_setprio 0
	s_barrier
	s_mov_b64 s[0:1], s[12:13]
	v_mov_b32_e32 v198, v139
	s_mov_b32 m0, s25
	ds_read_b128 v[166:169], v141 offset:16384
	ds_read_b128 v[170:173], v199 offset:16384
	ds_read_b128 v[174:177], v141 offset:18432
	ds_read_b128 v[178:181], v199 offset:18432
	ds_read_b128 v[182:185], v141 offset:20480
	ds_read_b128 v[186:189], v199 offset:20480
	ds_read_b128 v[190:193], v141 offset:22528
	ds_read_b128 v[194:197], v199 offset:22528
	s_nop 0
	global_load_lds_dwordx4 v198, s[0:1]
	s_add_u32 s0, s12, 0x40000
	s_addc_u32 s1, s13, 0
	v_mov_b32_e32 v198, v139
	s_mov_b32 m0, s26
	s_nop 0
	global_load_lds_dwordx4 v198, s[0:1]
	s_add_u32 s0, s12, 0x10000
	s_addc_u32 s1, s13, 0
	v_mov_b32_e32 v198, v139
	s_mov_b32 m0, s27
	s_nop 0
	global_load_lds_dwordx4 v198, s[0:1]
	s_add_u32 s0, s12, 0x50000
	s_addc_u32 s1, s13, 0
	v_mov_b32_e32 v198, v139
	s_mov_b32 m0, s28
	s_nop 0
	global_load_lds_dwordx4 v198, s[0:1]
	s_mov_b64 s[0:1], s[6:7]
	v_mov_b32_e32 v198, v138
	s_mov_b32 m0, s24
	s_nop 0
	global_load_lds_dwordx4 v198, s[0:1]
	s_add_u32 s0, s6, 0x20000
	s_addc_u32 s1, s7, 0
	v_mov_b32_e32 v198, v138
	s_mov_b32 m0, s29
	s_nop 0
	global_load_lds_dwordx4 v198, s[0:1]
	s_waitcnt vmcnt(8)
	s_waitcnt lgkmcnt(0)
	s_barrier
	s_setprio 1
	s_waitcnt lgkmcnt(0)
	v_mfma_f32_16x16x128_f8f6f4 v[70:73], v[2:9], v[166:173], v[70:73]
	v_mfma_f32_16x16x128_f8f6f4 v[66:69], v[142:149], v[166:173], v[66:69]
	v_mfma_f32_16x16x128_f8f6f4 v[54:57], v[2:9], v[174:181], v[54:57]
	v_mfma_f32_16x16x128_f8f6f4 v[50:53], v[142:149], v[174:181], v[50:53]
	v_mfma_f32_16x16x128_f8f6f4 v[38:41], v[2:9], v[182:189], v[38:41]
	v_mfma_f32_16x16x128_f8f6f4 v[34:37], v[142:149], v[182:189], v[34:37]
	v_mfma_f32_16x16x128_f8f6f4 v[2:5], v[2:9], v[190:197], v[22:25]
	v_mfma_f32_16x16x128_f8f6f4 v[6:9], v[142:149], v[190:197], v[18:21]
	s_setprio 0
	s_setprio 1
	v_mfma_f32_16x16x128_f8f6f4 v[62:65], v[150:157], v[166:173], v[62:65]
	v_mfma_f32_16x16x128_f8f6f4 v[58:61], v[158:165], v[166:173], v[58:61]
	v_mfma_f32_16x16x128_f8f6f4 v[46:49], v[150:157], v[174:181], v[46:49]
	v_mfma_f32_16x16x128_f8f6f4 v[42:45], v[158:165], v[174:181], v[42:45]
	v_mfma_f32_16x16x128_f8f6f4 v[30:33], v[150:157], v[182:189], v[30:33]
	v_mfma_f32_16x16x128_f8f6f4 v[26:29], v[158:165], v[182:189], v[26:29]
	v_mfma_f32_16x16x128_f8f6f4 v[14:17], v[150:157], v[190:197], v[14:17]
	v_mfma_f32_16x16x128_f8f6f4 v[10:13], v[158:165], v[190:197], v[10:13]
	s_setprio 0
	s_barrier
	ds_read_b128 v[18:21], v140 offset:32768
	ds_read_b128 v[22:25], v200 offset:32768
	ds_read_b128 v[142:145], v140 offset:34816
	ds_read_b128 v[146:149], v200 offset:34816
	ds_read_b128 v[150:153], v140 offset:49152
	ds_read_b128 v[154:157], v200 offset:49152
	ds_read_b128 v[158:161], v140 offset:51200
	ds_read_b128 v[162:165], v200 offset:51200
	s_add_u32 s0, s6, 0x40000
	s_addc_u32 s1, s7, 0
	v_mov_b32_e32 v198, v138
	s_mov_b32 m0, s30
	ds_read_b128 v[166:169], v141 offset:32768
	ds_read_b128 v[170:173], v199 offset:32768
	ds_read_b128 v[174:177], v141 offset:34816
	ds_read_b128 v[178:181], v199 offset:34816
	ds_read_b128 v[182:185], v141 offset:36864
	ds_read_b128 v[186:189], v199 offset:36864
	ds_read_b128 v[190:193], v141 offset:38912
	ds_read_b128 v[194:197], v199 offset:38912
	s_nop 0
	global_load_lds_dwordx4 v198, s[0:1]
	s_add_u32 s0, s6, 0x60000
	s_addc_u32 s1, s7, 0
	v_mov_b32_e32 v198, v138
	s_mov_b32 m0, s31
	s_nop 0
	global_load_lds_dwordx4 v198, s[0:1]
	s_waitcnt vmcnt(8)
	s_waitcnt lgkmcnt(0)
	s_barrier
	s_setprio 1
	s_waitcnt lgkmcnt(0)
	v_mfma_f32_16x16x128_f8f6f4 v[134:137], v[18:25], v[166:173], v[134:137]
	v_mfma_f32_16x16x128_f8f6f4 v[130:133], v[142:149], v[166:173], v[130:133]
	v_mfma_f32_16x16x128_f8f6f4 v[118:121], v[18:25], v[174:181], v[118:121]
	v_mfma_f32_16x16x128_f8f6f4 v[114:117], v[142:149], v[174:181], v[114:117]
	v_mfma_f32_16x16x128_f8f6f4 v[102:105], v[18:25], v[182:189], v[102:105]
	v_mfma_f32_16x16x128_f8f6f4 v[98:101], v[142:149], v[182:189], v[98:101]
	v_mfma_f32_16x16x128_f8f6f4 v[86:89], v[18:25], v[190:197], v[86:89]
	v_mfma_f32_16x16x128_f8f6f4 v[82:85], v[142:149], v[190:197], v[82:85]
	s_setprio 0
	s_setprio 1
	v_mfma_f32_16x16x128_f8f6f4 v[126:129], v[150:157], v[166:173], v[126:129]
	v_mfma_f32_16x16x128_f8f6f4 v[122:125], v[158:165], v[166:173], v[122:125]
	v_mfma_f32_16x16x128_f8f6f4 v[110:113], v[150:157], v[174:181], v[110:113]
	v_mfma_f32_16x16x128_f8f6f4 v[106:109], v[158:165], v[174:181], v[106:109]
	v_mfma_f32_16x16x128_f8f6f4 v[94:97], v[150:157], v[182:189], v[94:97]
	v_mfma_f32_16x16x128_f8f6f4 v[90:93], v[158:165], v[182:189], v[90:93]
	v_mfma_f32_16x16x128_f8f6f4 v[78:81], v[150:157], v[190:197], v[78:81]
	v_mfma_f32_16x16x128_f8f6f4 v[74:77], v[158:165], v[190:197], v[74:77]
	s_setprio 0
	s_barrier
	s_add_u32 s0, s12, 0x80
	s_addc_u32 s1, s13, 0
	v_mov_b32_e32 v198, v139
	s_mov_b32 m0, s35
	ds_read_b128 v[166:169], v141 offset:49152
	ds_read_b128 v[170:173], v199 offset:49152
	ds_read_b128 v[174:177], v141 offset:51200
	ds_read_b128 v[178:181], v199 offset:51200
	ds_read_b128 v[182:185], v141 offset:53248
	ds_read_b128 v[186:189], v199 offset:53248
	ds_read_b128 v[190:193], v141 offset:55296
	ds_read_b128 v[194:197], v199 offset:55296
	s_nop 0
	global_load_lds_dwordx4 v198, s[0:1]
	s_add_u32 s0, s12, 0x40080
	s_addc_u32 s1, s13, 0
	v_mov_b32_e32 v198, v139
	s_mov_b32 m0, s36
	s_nop 0
	global_load_lds_dwordx4 v198, s[0:1]
	s_add_u32 s0, s12, 0x10080
	s_addc_u32 s1, s13, 0
	v_mov_b32_e32 v198, v139
	s_mov_b32 m0, s57
	s_nop 0
	global_load_lds_dwordx4 v198, s[0:1]
	s_add_u32 s0, s12, 0x50080
	s_addc_u32 s1, s13, 0
	v_mov_b32_e32 v198, v139
	s_mov_b32 m0, s58
	s_nop 0
	global_load_lds_dwordx4 v198, s[0:1]
	v_mov_b32_e32 v198, v138
	s_mov_b32 m0, s37
	s_add_u32 s0, s6, 0x20080
	global_load_lds_dwordx4 v198, s[8:9]
	s_addc_u32 s1, s7, 0
	v_mov_b32_e32 v198, v138
	s_mov_b32 m0, s56
	s_nop 0
	global_load_lds_dwordx4 v198, s[0:1]
	s_waitcnt vmcnt(8)
	s_waitcnt lgkmcnt(0)
	s_barrier
	s_setprio 1
	s_waitcnt lgkmcnt(0)
	v_mfma_f32_16x16x128_f8f6f4 v[70:73], v[18:25], v[166:173], v[70:73]
	v_mfma_f32_16x16x128_f8f6f4 v[66:69], v[142:149], v[166:173], v[66:69]
	v_mfma_f32_16x16x128_f8f6f4 v[54:57], v[18:25], v[174:181], v[54:57]
	v_mfma_f32_16x16x128_f8f6f4 v[50:53], v[142:149], v[174:181], v[50:53]
	v_mfma_f32_16x16x128_f8f6f4 v[38:41], v[18:25], v[182:189], v[38:41]
	v_mfma_f32_16x16x128_f8f6f4 v[34:37], v[142:149], v[182:189], v[34:37]
	v_mfma_f32_16x16x128_f8f6f4 v[22:25], v[18:25], v[190:197], v[2:5]
	v_mfma_f32_16x16x128_f8f6f4 v[18:21], v[142:149], v[190:197], v[6:9]
	s_setprio 0
	s_setprio 1
	v_mfma_f32_16x16x128_f8f6f4 v[62:65], v[150:157], v[166:173], v[62:65]
	v_mfma_f32_16x16x128_f8f6f4 v[58:61], v[158:165], v[166:173], v[58:61]
	v_mfma_f32_16x16x128_f8f6f4 v[46:49], v[150:157], v[174:181], v[46:49]
	v_mfma_f32_16x16x128_f8f6f4 v[42:45], v[158:165], v[174:181], v[42:45]
	v_mfma_f32_16x16x128_f8f6f4 v[30:33], v[150:157], v[182:189], v[30:33]
	v_mfma_f32_16x16x128_f8f6f4 v[26:29], v[158:165], v[182:189], v[26:29]
	v_mfma_f32_16x16x128_f8f6f4 v[14:17], v[150:157], v[190:197], v[14:17]
	v_mfma_f32_16x16x128_f8f6f4 v[10:13], v[158:165], v[190:197], v[10:13]
	s_setprio 0
	s_barrier
	s_add_i32 s65, s65, 2
	s_add_u32 s63, s63, 0x100
	s_addc_u32 s64, s64, 0
	s_cmp_gt_u32 s65, 13
	s_mov_b64 s[0:1], s[4:5]
	s_cbranch_scc0 .LBB0_1350
	s_and_b64 vcc, exec, s[44:45]
	s_cbranch_vccz .LBB0_1353
	s_barrier
